# v23 with streaming (nt) policy on the final output stores of phase 9 (written once, never re-read; keeps Y / x1 in the caches)
# baseline (speedup 1.0000x reference)
.LBB0_923:
	s_add_i32 s21, s54, s52
	s_cmpk_lt_i32 s21, 0x4000
	s_cselect_b32 s12, s21, s52
	s_add_i32 s22, s8, -3
	s_ashr_i32 s13, s12, 31
	s_ashr_i32 s23, s22, 31
	s_lshl_b64 s[0:1], s[12:13], 12
	s_lshl_b32 s24, s12, 2
	s_lshl_b64 s[22:23], s[22:23], 2
	s_add_u32 s26, s14, s22
	s_addc_u32 s27, s15, s23
	s_add_u32 s22, s16, s22
	s_addc_u32 s23, s17, s23
	s_ashr_i32 s25, s24, 31
	global_load_dword v53, v37, s[26:27]
	global_load_dword v52, v37, s[22:23]
	s_lshl_b64 s[22:23], s[24:25], 2
	s_add_u32 s24, s14, s22
	s_addc_u32 s25, s15, s23
	s_add_u32 s22, s16, s22
	s_addc_u32 s23, s17, s23
	global_load_dwordx4 v[46:49], v37, s[24:25]
	global_load_dwordx4 v[32:35], v37, s[22:23]
	s_add_i32 s22, s8, -2
	s_ashr_i32 s23, s22, 31
	s_lshl_b64 s[22:23], s[22:23], 2
	s_add_u32 s24, s14, s22
	s_addc_u32 s25, s15, s23
	s_add_u32 s22, s16, s22
	s_addc_u32 s23, s17, s23
	global_load_dword v57, v37, s[24:25]
	global_load_dword v56, v37, s[22:23]
	s_add_i32 s22, s8, -1
	s_ashr_i32 s23, s22, 31
	s_lshl_b64 s[22:23], s[22:23], 2
	s_add_u32 s24, s14, s22
	s_addc_u32 s25, s15, s23
	global_load_dword v59, v37, s[24:25]
	s_add_u32 s22, s16, s22
	s_addc_u32 s23, s17, s23
	s_ashr_i32 s9, s8, 31
	global_load_dword v58, v37, s[22:23]
	s_lshl_b64 s[22:23], s[8:9], 2
	s_add_u32 s24, s14, s22
	s_addc_u32 s25, s15, s23
	global_load_dword v61, v37, s[24:25]
	s_add_u32 s22, s16, s22
	s_addc_u32 s23, s17, s23
	global_load_dword v60, v37, s[22:23]
	global_load_dwordx2 v[54:55], v[44:45], off offset:2048
	global_load_dwordx2 v[50:51], v[44:45], off offset:2560
	global_load_dwordx2 v[64:65], v[44:45], off offset:3072
	global_load_dwordx2 v[66:67], v[44:45], off offset:3584
	s_cmpk_gt_i32 s21, 0x3fff
	s_waitcnt vmcnt(13)
	v_lshlrev_b32_e32 v53, 2, v53
	v_add_u32_e32 v68, s5, v53
	s_waitcnt vmcnt(12)
	v_ashrrev_i32_e32 v53, 31, v52
	v_lshlrev_b64 v[62:63], 11, v[52:53]
	s_waitcnt vmcnt(11)
	v_lshlrev_b32_e32 v46, 2, v46
	v_lshlrev_b32_e32 v47, 2, v47
	v_lshlrev_b32_e32 v48, 2, v48
	v_lshlrev_b32_e32 v49, 2, v49
	v_add_u32_e32 v52, s5, v46
	v_add_u32_e32 v53, s5, v47
	v_add_u32_e32 v69, s5, v48
	v_add_u32_e32 v71, s5, v49
	s_waitcnt vmcnt(10)
	v_ashrrev_i32_e32 v47, 31, v32
	v_mov_b32_e32 v46, v32
	v_ashrrev_i32_e32 v49, 31, v33
	v_mov_b32_e32 v48, v33
	ds_read_b32 v32, v68
	ds_read_b32 v52, v52
	ds_read_b32 v68, v53
	ds_read_b32 v70, v69
	ds_read_b32 v72, v71
	s_waitcnt vmcnt(9)
	v_lshlrev_b32_e32 v33, 2, v57
	v_add_u32_e32 v33, s5, v33
	s_waitcnt lgkmcnt(3)
	v_ashrrev_i32_e32 v53, 31, v52
	ds_read_b32 v74, v33
	v_ashrrev_i32_e32 v33, 31, v32
	v_lshlrev_b64 v[52:53], 19, v[52:53]
	v_lshlrev_b64 v[32:33], 19, v[32:33]
	v_lshlrev_b64 v[46:47], 11, v[46:47]
	s_waitcnt lgkmcnt(3)
	v_ashrrev_i32_e32 v69, 31, v68
	s_waitcnt vmcnt(8)
	v_ashrrev_i32_e32 v57, 31, v56
	v_lshl_add_u64 v[52:53], s[2:3], 0, v[52:53]
	v_lshl_add_u64 v[32:33], s[2:3], 0, v[32:33]
	v_lshlrev_b64 v[68:69], 19, v[68:69]
	v_lshlrev_b64 v[76:77], 11, v[56:57]
	v_lshl_add_u64 v[56:57], v[52:53], 0, v[46:47]
	v_lshl_add_u64 v[32:33], v[32:33], 0, v[62:63]
	s_waitcnt vmcnt(7)
	v_lshlrev_b32_e32 v46, 2, v59
	v_lshlrev_b64 v[48:49], 11, v[48:49]
	v_lshl_add_u64 v[68:69], s[2:3], 0, v[68:69]
	v_readfirstlane_b32 s22, v32
	v_readfirstlane_b32 s23, v33
	v_add_u32_e32 v32, s5, v46
	v_lshl_add_u64 v[52:53], v[68:69], 0, v[48:49]
	s_nop 2
	global_load_dword v68, v36, s[22:23]
	global_load_dword v69, v36, s[22:23] offset:256
	global_load_dword v78, v36, s[22:23] offset:512
	ds_read_b32 v32, v32
	s_waitcnt vmcnt(8)
	v_lshlrev_b32_e32 v33, 2, v61
	s_waitcnt lgkmcnt(1)
	v_ashrrev_i32_e32 v75, 31, v74
	v_add_u32_e32 v33, s5, v33
	v_lshlrev_b64 v[46:47], 19, v[74:75]
	ds_read_b32 v62, v33
	s_waitcnt lgkmcnt(1)
	v_ashrrev_i32_e32 v33, 31, v32
	v_ashrrev_i32_e32 v59, 31, v58
	v_lshl_add_u64 v[46:47], s[2:3], 0, v[46:47]
	v_lshlrev_b64 v[32:33], 19, v[32:33]
	v_lshlrev_b64 v[48:49], 11, v[58:59]
	v_lshl_add_u64 v[46:47], v[46:47], 0, v[76:77]
	v_lshl_add_u64 v[32:33], s[2:3], 0, v[32:33]
	v_lshl_add_u64 v[32:33], v[32:33], 0, v[48:49]
	global_load_dword v76, v36, s[22:23] offset:768
	global_load_dword v77, v36, s[22:23] offset:1024
	global_load_dword v79, v36, s[22:23] offset:1280
	global_load_dword v84, v36, s[22:23] offset:1536
	global_load_dword v85, v36, s[22:23] offset:1792
	v_readfirstlane_b32 s22, v46
	v_readfirstlane_b32 s23, v47
	v_ashrrev_i32_e32 v71, 31, v70
	v_ashrrev_i32_e32 v49, 31, v34
	v_mov_b32_e32 v48, v34
	v_lshlrev_b64 v[58:59], 19, v[70:71]
	v_lshlrev_b64 v[48:49], 11, v[48:49]
	global_load_dword v86, v36, s[22:23]
	global_load_dword v87, v36, s[22:23] offset:256
	global_load_dword v90, v36, s[22:23] offset:512
	global_load_dword v91, v36, s[22:23] offset:768
	global_load_dword v92, v36, s[22:23] offset:1024
	global_load_dword v93, v36, s[22:23] offset:1280
	global_load_dword v96, v36, s[22:23] offset:1536
	global_load_dword v97, v36, s[22:23] offset:1792
	v_readfirstlane_b32 s22, v32
	v_readfirstlane_b32 s23, v33
	v_lshl_add_u64 v[58:59], s[2:3], 0, v[58:59]
	s_waitcnt lgkmcnt(0)
	v_ashrrev_i32_e32 v63, 31, v62
	v_lshl_add_u64 v[58:59], v[58:59], 0, v[48:49]
	s_waitcnt vmcnt(20)
	v_ashrrev_i32_e32 v61, 31, v60
	v_lshlrev_b64 v[48:49], 19, v[62:63]
	global_load_dword v156, v36, s[22:23]
	global_load_dword v160, v36, s[22:23] offset:256
	v_lshlrev_b64 v[46:47], 11, v[60:61]
	v_lshl_add_u64 v[48:49], s[2:3], 0, v[48:49]
	v_ashrrev_i32_e32 v73, 31, v72
	v_lshl_add_u64 v[46:47], v[48:49], 0, v[46:47]
	v_ashrrev_i32_e32 v49, 31, v35
	v_mov_b32_e32 v48, v35
	v_lshlrev_b64 v[34:35], 19, v[72:73]
	global_load_dword v164, v36, s[22:23] offset:512
	global_load_dword v168, v36, s[22:23] offset:768
	global_load_dword v170, v36, s[22:23] offset:1024
	global_load_dword v178, v36, s[22:23] offset:1280
	global_load_dword v176, v36, s[22:23] offset:1536
	global_load_dwordx2 v[94:95], v[44:45], off
	global_load_dwordx2 v[70:71], v[44:45], off offset:512
	global_load_dwordx2 v[80:81], v[44:45], off offset:1024
	global_load_dwordx2 v[82:83], v[44:45], off offset:1536
	global_load_dword v179, v36, s[22:23] offset:1792
	v_lshlrev_b64 v[48:49], 11, v[48:49]
	v_lshl_add_u64 v[34:35], s[2:3], 0, v[34:35]
	v_lshl_add_u64 v[62:63], v[38:39], 0, s[0:1]
	v_readfirstlane_b32 s0, v46
	v_readfirstlane_b32 s1, v47
	v_lshl_add_u64 v[60:61], v[34:35], 0, v[48:49]
	s_nop 3
	global_load_dword v182, v36, s[0:1]
	global_load_dwordx2 v[32:33], v[62:63], off
	global_load_dwordx2 v[48:49], v[62:63], off offset:512
	global_load_dwordx2 v[46:47], v[62:63], off offset:1024
	global_load_dwordx2 v[34:35], v[62:63], off offset:1536
	global_load_dword v186, v36, s[0:1] offset:256
	global_load_dword v190, v36, s[0:1] offset:512
	global_load_dword v194, v36, s[0:1] offset:768
	global_load_dword v196, v36, s[0:1] offset:1024
	global_load_dword v204, v36, s[0:1] offset:1280
	global_load_dword v202, v36, s[0:1] offset:1536
	global_load_dword v205, v36, s[0:1] offset:1792
	s_waitcnt vmcnt(41)
	v_lshlrev_b32_e32 v102, 16, v64
	v_and_b32_e32 v104, 0xffff0000, v64
	v_lshlrev_b32_e32 v105, 16, v65
	v_and_b32_e32 v126, 0xffff0000, v65
	s_waitcnt vmcnt(40)
	v_lshlrev_b32_e32 v210, 16, v66
	v_and_b32_e32 v99, 0xffff0000, v66
	v_lshlrev_b32_e32 v107, 16, v67
	v_and_b32_e32 v103, 0xffff0000, v67
	v_lshlrev_b32_e32 v98, 16, v50
	v_and_b32_e32 v50, 0xffff0000, v50
	v_readfirstlane_b32 s0, v56
	v_readfirstlane_b32 s1, v57
	s_waitcnt vmcnt(39)
	v_cvt_pk_f32_fp8_e32 v[108:109], v68
	s_waitcnt vmcnt(38)
	v_cvt_pk_f32_fp8_e32 v[64:65], v69
	v_cvt_pk_f32_fp8_sdwa v[74:75], v69 src0_sel:WORD_1
	s_waitcnt vmcnt(37)
	v_cvt_pk_f32_fp8_e32 v[88:89], v78
	v_cvt_pk_f32_fp8_sdwa v[100:101], v78 src0_sel:WORD_1
	v_mov_b32_e32 v208, v64
	v_mov_b32_e32 v209, v74
	v_mov_b32_e32 v74, v65
	v_cvt_pk_f32_fp8_sdwa v[120:121], v68 src0_sel:WORD_1
	s_waitcnt vmcnt(36)
	v_cvt_pk_f32_fp8_e32 v[110:111], v76
	v_cvt_pk_f32_fp8_sdwa v[122:123], v76 src0_sel:WORD_1
	s_waitcnt vmcnt(35)
	v_cvt_pk_f32_fp8_e32 v[68:69], v77
	s_waitcnt vmcnt(34)
	v_cvt_pk_f32_fp8_e32 v[72:73], v79
	v_cvt_pk_f32_fp8_sdwa v[124:125], v77 src0_sel:WORD_1
	v_cvt_pk_f32_fp8_sdwa v[66:67], v79 src0_sel:WORD_1
	s_waitcnt vmcnt(33)
	v_cvt_pk_f32_fp8_e32 v[76:77], v84
	v_cvt_pk_f32_fp8_sdwa v[78:79], v84 src0_sel:WORD_1
	v_add_f32_e32 v98, v72, v98
	v_add_f32_e32 v50, v73, v50
	v_add_f32_e32 v106, v76, v102
	s_waitcnt vmcnt(31)
	v_cvt_pk_f32_fp8_e32 v[128:129], v86
	s_waitcnt vmcnt(30)
	v_cvt_pk_f32_fp8_e32 v[132:133], v87
	v_cvt_pk_f32_fp8_sdwa v[134:135], v87 src0_sel:WORD_1
	s_waitcnt vmcnt(29)
	v_cvt_pk_f32_fp8_e32 v[136:137], v90
	v_cvt_pk_f32_fp8_sdwa v[138:139], v90 src0_sel:WORD_1
	s_waitcnt vmcnt(28)
	v_cvt_pk_f32_fp8_e32 v[140:141], v91
	v_cvt_pk_f32_fp8_sdwa v[142:143], v91 src0_sel:WORD_1
	v_cvt_pk_f32_fp8_sdwa v[130:131], v86 src0_sel:WORD_1
	s_waitcnt vmcnt(25)
	v_cvt_pk_f32_fp8_sdwa v[148:149], v96 src0_sel:WORD_1
	v_add_f32_e32 v84, v77, v104
	v_add_f32_e32 v102, v78, v105
	v_add_f32_e32 v150, v79, v126
	v_cvt_pk_f32_fp8_e32 v[104:105], v85
	v_cvt_pk_f32_fp8_e32 v[78:79], v93
	v_cvt_pk_f32_fp8_e32 v[146:147], v96
	s_waitcnt vmcnt(21)
	v_cvt_pk_f32_fp8_e32 v[162:163], v164
	v_cvt_pk_f32_fp8_e32 v[158:159], v160
	v_cvt_pk_f32_fp8_sdwa v[160:161], v160 src0_sel:WORD_1
	v_cvt_pk_f32_fp8_sdwa v[164:165], v164 src0_sel:WORD_1
	v_cvt_pk_f32_fp8_e32 v[154:155], v156
	s_waitcnt vmcnt(11)
	v_cvt_pk_f32_fp8_e32 v[180:181], v182
	v_lshlrev_b32_e32 v207, 16, v71
	v_lshlrev_b32_e32 v206, 16, v70
	v_and_b32_e32 v71, 0xffff0000, v71
	v_and_b32_e32 v70, 0xffff0000, v70
	s_waitcnt vmcnt(6)
	v_cvt_pk_f32_fp8_e32 v[184:185], v186
	v_cvt_pk_f32_fp8_sdwa v[186:187], v186 src0_sel:WORD_1
	v_pk_add_f32 v[206:207], v[208:209], v[206:207]
	v_pk_add_f32 v[64:65], v[74:75], v[70:71]
	v_mov_b32_e32 v70, v132
	v_mov_b32_e32 v71, v134
	v_mov_b32_e32 v134, v133
	v_pk_add_f32 v[70:71], v[206:207], v[70:71]
	v_pk_add_f32 v[64:65], v[64:65], v[134:135]
	v_mov_b32_e32 v74, v158
	v_mov_b32_e32 v75, v160
	v_mov_b32_e32 v160, v159
	v_pk_add_f32 v[70:71], v[70:71], v[74:75]
	v_pk_add_f32 v[64:65], v[64:65], v[160:161]
	v_mov_b32_e32 v75, v186
	v_mov_b32_e32 v186, v185
	v_mov_b32_e32 v74, v184
	v_pk_add_f32 v[64:65], v[64:65], v[186:187]
	v_pk_add_f32 v[74:75], v[70:71], v[74:75]
	v_pk_mul_f32 v[70:71], v[64:65], v[64:65]
	s_waitcnt vmcnt(5)
	v_cvt_pk_f32_fp8_e32 v[188:189], v190
	v_cvt_pk_f32_fp8_sdwa v[190:191], v190 src0_sel:WORD_1
	v_pk_fma_f32 v[70:71], v[74:75], v[74:75], v[70:71]
	v_mov_b32_e32 v134, v88
	v_pk_add_f32 v[132:133], v[70:71], v[70:71] op_sel:[0,1] op_sel_hi:[1,0]
	v_lshlrev_b32_e32 v71, 16, v81
	v_lshlrev_b32_e32 v70, 16, v80
	v_and_b32_e32 v81, 0xffff0000, v81
	v_and_b32_e32 v80, 0xffff0000, v80
	v_mov_b32_e32 v135, v100
	v_mov_b32_e32 v100, v89
	v_pk_add_f32 v[70:71], v[134:135], v[70:71]
	v_pk_add_f32 v[80:81], v[100:101], v[80:81]
	v_mov_b32_e32 v88, v136
	v_mov_b32_e32 v89, v138
	v_mov_b32_e32 v138, v137
	v_mov_b32_e32 v100, v110
	v_mov_b32_e32 v101, v122
	v_mov_b32_e32 v122, v111
	v_lshlrev_b32_e32 v110, 16, v94
	v_and_b32_e32 v111, 0xffff0000, v94
	v_pk_add_f32 v[70:71], v[70:71], v[88:89]
	v_pk_add_f32 v[80:81], v[80:81], v[138:139]
	v_mov_b32_e32 v88, v162
	v_mov_b32_e32 v89, v164
	v_mov_b32_e32 v164, v163
	v_pk_add_f32 v[108:109], v[108:109], v[110:111]
	v_pk_add_f32 v[70:71], v[70:71], v[88:89]
	v_pk_add_f32 v[80:81], v[80:81], v[164:165]
	v_mov_b32_e32 v88, v188
	v_mov_b32_e32 v89, v190
	v_mov_b32_e32 v190, v189
	v_pk_add_f32 v[108:109], v[108:109], v[128:129]
	v_pk_add_f32 v[88:89], v[70:71], v[88:89]
	v_pk_add_f32 v[70:71], v[80:81], v[190:191]
	v_pk_add_f32 v[108:109], v[108:109], v[154:155]
	v_cvt_pk_f32_fp8_e32 v[166:167], v168
	v_cvt_pk_f32_fp8_sdwa v[168:169], v168 src0_sel:WORD_1
	v_pk_mul_f32 v[80:81], v[70:71], v[70:71]
	v_pk_add_f32 v[110:111], v[108:109], v[180:181]
	v_cvt_pk_f32_fp8_sdwa v[156:157], v156 src0_sel:WORD_1
	s_waitcnt vmcnt(4)
	v_cvt_pk_f32_fp8_e32 v[192:193], v194
	v_cvt_pk_f32_fp8_sdwa v[194:195], v194 src0_sel:WORD_1
	v_pk_fma_f32 v[80:81], v[88:89], v[88:89], v[80:81]
	v_mul_f32_e32 v94, v111, v111
	v_cvt_pk_f32_fp8_sdwa v[182:183], v182 src0_sel:WORD_1
	v_pk_add_f32 v[134:135], v[80:81], v[80:81] op_sel:[0,1] op_sel_hi:[1,0]
	v_lshlrev_b32_e32 v81, 16, v83
	v_lshlrev_b32_e32 v80, 16, v82
	v_and_b32_e32 v83, 0xffff0000, v83
	v_and_b32_e32 v82, 0xffff0000, v82
	v_pk_fma_f32 v[108:109], v[110:111], v[110:111], v[94:95] op_sel_hi:[1,1,0]
	v_lshlrev_b32_e32 v94, 16, v95
	v_and_b32_e32 v95, 0xffff0000, v95
	v_pk_add_f32 v[80:81], v[100:101], v[80:81]
	v_pk_add_f32 v[82:83], v[122:123], v[82:83]
	v_mov_b32_e32 v100, v140
	v_mov_b32_e32 v101, v142
	v_mov_b32_e32 v142, v141
	v_pk_add_f32 v[94:95], v[120:121], v[94:95]
	v_cvt_pk_f32_fp8_sdwa v[126:127], v85 src0_sel:WORD_1
	v_cvt_pk_f32_fp8_e32 v[172:173], v178
	v_cvt_pk_f32_fp8_e32 v[174:175], v176
	v_cvt_pk_f32_fp8_sdwa v[176:177], v176 src0_sel:WORD_1
	v_pk_add_f32 v[80:81], v[80:81], v[100:101]
	v_pk_add_f32 v[82:83], v[82:83], v[142:143]
	v_mov_b32_e32 v100, v166
	v_mov_b32_e32 v101, v168
	v_mov_b32_e32 v168, v167
	v_pk_add_f32 v[94:95], v[94:95], v[130:131]
	v_add_f32_e32 v87, v150, v149
	v_cvt_pk_f32_fp8_e32 v[150:151], v97
	v_cvt_pk_f32_fp8_sdwa v[152:153], v97 src0_sel:WORD_1
	s_waitcnt vmcnt(2)
	v_cvt_pk_f32_fp8_e32 v[198:199], v204
	s_waitcnt vmcnt(1)
	v_cvt_pk_f32_fp8_e32 v[200:201], v202
	v_cvt_pk_f32_fp8_sdwa v[202:203], v202 src0_sel:WORD_1
	v_pk_add_f32 v[80:81], v[80:81], v[100:101]
	v_pk_add_f32 v[82:83], v[82:83], v[168:169]
	v_mov_b32_e32 v100, v192
	v_mov_b32_e32 v101, v194
	v_mov_b32_e32 v194, v193
	v_pk_add_f32 v[94:95], v[94:95], v[156:157]
	v_pk_add_f32 v[100:101], v[80:81], v[100:101]
	v_pk_add_f32 v[80:81], v[82:83], v[194:195]
	v_pk_add_f32 v[140:141], v[94:95], v[182:183]
	v_cvt_pk_f32_fp8_sdwa v[144:145], v92 src0_sel:WORD_1
	v_add_f32_e32 v98, v98, v78
	v_add_f32_e32 v50, v50, v79
	v_add_f32_e32 v86, v84, v147
	v_cvt_pk_f32_fp8_sdwa v[78:79], v178 src0_sel:WORD_1
	v_cvt_pk_f32_fp8_e32 v[90:91], v179
	v_cvt_pk_f32_fp8_sdwa v[178:179], v179 src0_sel:WORD_1
	v_pk_mul_f32 v[82:83], v[80:81], v[80:81]
	v_mov_b32_e32 v109, v104
	v_mul_f32_e32 v104, v141, v141
	v_cvt_pk_f32_fp8_e32 v[84:85], v170
	v_cvt_pk_f32_fp8_sdwa v[170:171], v170 src0_sel:WORD_1
	v_add_f32_e32 v50, v50, v173
	v_add_f32_e32 v86, v86, v175
	v_add_f32_e32 v87, v87, v177
	v_pk_fma_f32 v[82:83], v[100:101], v[100:101], v[82:83]
	v_mov_b32_e32 v149, v127
	v_mov_b32_e32 v173, v105
	v_pk_fma_f32 v[104:105], v[140:141], v[140:141], v[104:105] op_sel_hi:[1,1,0]
	v_cvt_pk_f32_fp8_e32 v[96:97], v196
	v_cvt_pk_f32_fp8_sdwa v[196:197], v196 src0_sel:WORD_1
	v_add_f32_e32 v211, v50, v199
	v_add_f32_e32 v212, v86, v201
	v_add_f32_e32 v213, v87, v203
	s_waitcnt vmcnt(0)
	v_cvt_pk_f32_fp8_e32 v[86:87], v205
	v_pk_add_f32 v[122:123], v[82:83], v[82:83] op_sel:[0,1] op_sel_hi:[1,0]
	v_lshlrev_b32_e32 v82, 16, v55
	v_and_b32_e32 v83, 0xffff0000, v55
	v_mov_b32_e32 v147, v126
	v_pk_add_f32 v[102:103], v[102:103], v[148:149]
	v_pk_add_f32 v[98:99], v[98:99], v[172:173]
	v_mov_b32_e32 v177, v153
	v_mov_b32_e32 v199, v151
	v_mov_b32_e32 v105, v210
	v_cvt_pk_f32_fp8_e32 v[76:77], v92
	v_cvt_pk_f32_fp8_sdwa v[72:73], v93 src0_sel:WORD_1
	v_cvt_pk_f32_fp8_sdwa v[92:93], v204 src0_sel:WORD_1
	v_cvt_pk_f32_fp8_sdwa v[204:205], v205 src0_sel:WORD_1
	v_pk_add_f32 v[82:83], v[124:125], v[82:83]
	v_pk_add_f32 v[94:95], v[106:107], v[146:147]
	v_pk_add_f32 v[106:107], v[102:103], v[176:177]
	v_pk_add_f32 v[102:103], v[98:99], v[198:199]
	v_pk_add_f32 v[104:105], v[108:109], v[104:105]
	v_mov_b32_e32 v133, v150
	v_pk_add_f32 v[82:83], v[82:83], v[144:145]
	v_mov_b32_e32 v175, v152
	v_mov_b32_e32 v203, v179
	v_pk_add_f32 v[120:121], v[104:105], v[132:133]
	v_mov_b32_e32 v104, v102
	v_mov_b32_e32 v105, v91
	v_pk_add_f32 v[82:83], v[82:83], v[170:171]
	v_pk_add_f32 v[94:95], v[94:95], v[174:175]
	v_mov_b32_e32 v201, v178
	v_pk_add_f32 v[98:99], v[106:107], v[202:203]
	v_pk_mul_f32 v[106:107], v[102:103], v[102:103]
	v_pk_add_f32 v[128:129], v[102:103], v[104:105]
	v_pk_add_f32 v[82:83], v[82:83], v[196:197]
	v_mul_f32_e32 v136, v211, v211
	v_pk_add_f32 v[94:95], v[94:95], v[200:201]
	v_mov_b32_e32 v107, v129
	v_mov_b32_e32 v137, v87
	v_mul_f32_e32 v50, v83, v83
	v_pk_add_f32 v[104:105], v[106:107], v[136:137]
	v_mov_b32_e32 v106, v94
	v_mov_b32_e32 v107, v204
	v_pk_fma_f32 v[124:125], v[82:83], v[82:83], v[50:51] op_sel_hi:[1,1,0]
	v_mul_f32_e32 v50, v212, v212
	v_pk_add_f32 v[106:107], v[94:95], v[106:107]
	v_mov_b32_e32 v204, v98
	v_mul_f32_e32 v138, v213, v213
	v_mov_b32_e32 v135, v90
	v_pk_add_f32 v[108:109], v[98:99], v[204:205]
	v_pk_fma_f32 v[130:131], v[94:95], v[94:95], v[50:51]
	v_pk_mul_f32 v[132:133], v[106:107], v[106:107]
	v_pk_add_f32 v[126:127], v[120:121], v[134:135]
	v_mov_b32_e32 v131, v133
	v_pk_fma_f32 v[132:133], v[98:99], v[98:99], v[138:139]
	v_pk_mul_f32 v[134:135], v[108:109], v[108:109]
	v_mov_b32_e32 v123, v86
	v_mov_b32_e32 v133, v135
	v_pk_add_f32 v[130:131], v[130:131], v[132:133]
	v_pk_add_f32 v[132:133], v[126:127], v[122:123]
	v_lshlrev_b32_e32 v122, 16, v54
	v_and_b32_e32 v123, 0xffff0000, v54
	v_pk_add_f32 v[54:55], v[68:69], v[122:123]
	v_lshlrev_b32_e32 v50, 16, v51
	v_pk_add_f32 v[54:55], v[54:55], v[76:77]
	v_and_b32_e32 v51, 0xffff0000, v51
	v_pk_add_f32 v[54:55], v[54:55], v[84:85]
	v_pk_add_f32 v[50:51], v[66:67], v[50:51]
	v_pk_add_f32 v[134:135], v[54:55], v[96:97]
	v_pk_add_f32 v[50:51], v[50:51], v[72:73]
	v_pk_mul_f32 v[54:55], v[134:135], v[134:135]
	v_pk_add_f32 v[50:51], v[50:51], v[78:79]
	v_mov_b32_e32 v120, v54
	v_pk_mov_b32 v[54:55], v[54:55], v[90:91] op_sel:[1,0]
	v_pk_add_f32 v[136:137], v[50:51], v[92:93]
	v_mov_b32_e32 v125, v86
	v_pk_add_f32 v[54:55], v[120:121], v[54:55]
	v_pk_mul_f32 v[50:51], v[136:137], v[136:137]
	v_pk_add_f32 v[54:55], v[54:55], v[124:125]
	v_mov_b32_e32 v128, v50
	v_mov_b32_e32 v86, v51
	v_pk_add_f32 v[68:69], v[132:133], v[54:55]
	v_pk_mul_f32 v[54:55], v[132:133], v[54:55]
	v_pk_add_f32 v[50:51], v[128:129], v[86:87]
	v_mov_b32_e32 v69, v55
	v_pk_add_f32 v[54:55], v[104:105], v[50:51]
	v_pk_mul_f32 v[50:51], v[104:105], v[50:51]
	v_mov_b32_e32 v103, v211
	v_mov_b32_e32 v55, v51
	v_pk_add_f32 v[50:51], v[68:69], v[54:55]
	v_mov_b32_e32 v95, v212
	v_pk_add_f32 v[50:51], v[50:51], v[130:131]
	v_mov_b32_e32 v99, v213
	v_add_f32_e32 v72, v50, v51
	ds_bpermute_b32 v73, v112, v72
	global_load_dwordx2 v[54:55], v[62:63], off offset:2048
	global_load_dwordx2 v[50:51], v[62:63], off offset:2560
	global_load_dwordx2 v[68:69], v[62:63], off offset:3072
	global_load_dwordx2 v[66:67], v[62:63], off offset:3584
	global_load_dword v132, v36, s[0:1]
	global_load_dword v131, v36, s[0:1] offset:256
	global_load_dword v57, v36, s[0:1] offset:512
	global_load_dword v56, v36, s[0:1] offset:768
	global_load_dword v79, v36, s[0:1] offset:1024
	global_load_dword v84, v36, s[0:1] offset:1280
	global_load_dword v78, v36, s[0:1] offset:1536
	global_load_dword v125, v36, s[0:1] offset:1792
	v_readfirstlane_b32 s0, v52
	v_readfirstlane_b32 s1, v53
	s_waitcnt lgkmcnt(0)
	v_add_f32_e32 v62, v72, v73
	ds_bpermute_b32 v63, v113, v62
	s_nop 1
	global_load_dword v130, v36, s[0:1]
	global_load_dword v129, v36, s[0:1] offset:256
	global_load_dword v128, v36, s[0:1] offset:512
	global_load_dword v127, v36, s[0:1] offset:768
	global_load_dword v126, v36, s[0:1] offset:1024
	global_load_dword v124, v36, s[0:1] offset:1280
	global_load_dword v76, v36, s[0:1] offset:1536
	global_load_dword v97, v36, s[0:1] offset:1792
	v_readfirstlane_b32 s0, v58
	v_readfirstlane_b32 s1, v59
	v_mov_b32_e32 v104, v133
	s_waitcnt lgkmcnt(0)
	v_add_f32_e32 v52, v62, v63
	s_nop 1
	global_load_dword v123, v36, s[0:1]
	global_load_dword v122, v36, s[0:1] offset:256
	global_load_dword v121, v36, s[0:1] offset:512
	global_load_dword v120, v36, s[0:1] offset:768
	global_load_dword v106, v36, s[0:1] offset:1024
	global_load_dword v62, v36, s[0:1] offset:1280
	global_load_dword v63, v36, s[0:1] offset:1536
	global_load_dword v87, v36, s[0:1] offset:1792
	v_readfirstlane_b32 s0, v60
	v_readfirstlane_b32 s1, v61
	s_nop 4
	global_load_dword v96, v36, s[0:1]
	global_load_dword v93, v36, s[0:1] offset:256
	global_load_dword v92, v36, s[0:1] offset:512
	global_load_dword v91, v36, s[0:1] offset:768
	global_load_dword v90, v36, s[0:1] offset:1024
	global_load_dword v73, v36, s[0:1] offset:1280
	global_load_dword v86, v36, s[0:1] offset:1536
	global_load_dword v72, v36, s[0:1] offset:1792
	ds_bpermute_b32 v53, v114, v52
	v_mov_b32_e32 v108, v107
	s_waitcnt lgkmcnt(0)
	v_add_f32_e32 v52, v52, v53
	ds_bpermute_b32 v53, v115, v52
	s_waitcnt lgkmcnt(0)
	v_add_f32_e32 v52, v52, v53
	ds_bpermute_b32 v53, v116, v52
	s_waitcnt lgkmcnt(0)
	v_add_f32_e32 v58, v52, v53
	ds_bpermute_b32 v59, v117, v58
	v_mov_b32_e32 v52, v74
	v_mov_b32_e32 v74, v88
	v_mov_b32_e32 v88, v100
	v_mov_b32_e32 v53, v64
	s_waitcnt lgkmcnt(0)
	v_add_f32_e32 v58, v58, v59
	v_fmamk_f32 v58, v58, 0x3a000000, v118
	v_mul_f32_e32 v59, 0x4f800000, v58
	v_cmp_gt_f32_e32 vcc, s20, v58
	v_mov_b32_e32 v64, v75
	v_mov_b32_e32 v75, v70
	v_cndmask_b32_e32 v58, v58, v59, vcc
	v_sqrt_f32_e32 v59, v58
	v_mov_b32_e32 v70, v89
	v_mov_b32_e32 v89, v80
	v_mov_b32_e32 v80, v101
	v_add_u32_e32 v60, -1, v59
	v_fma_f32 v61, -v60, v59, v58
	v_cmp_ge_f32_e64 s[0:1], 0, v61
	v_add_u32_e32 v61, 1, v59
	s_nop 0
	v_cndmask_b32_e64 v60, v59, v60, s[0:1]
	v_fma_f32 v59, -v61, v59, v58
	v_cmp_lt_f32_e64 s[0:1], 0, v59
	s_nop 1
	v_cndmask_b32_e64 v59, v60, v61, s[0:1]
	v_mul_f32_e32 v60, 0x37800000, v59
	v_cndmask_b32_e32 v59, v59, v60, vcc
	v_cmp_class_f32_e32 vcc, v58, v119
	s_nop 1
	v_cndmask_b32_e32 v58, v59, v58, vcc
	v_div_scale_f32 v59, s[0:1], v58, v58, 1.0
	v_rcp_f32_e32 v60, v59
	s_nop 0
	v_fma_f32 v61, -v59, v60, 1.0
	v_fmac_f32_e32 v60, v61, v60
	v_div_scale_f32 v61, vcc, 1.0, v58, 1.0
	v_mul_f32_e32 v77, v61, v60
	v_fma_f32 v85, -v59, v77, v61
	v_fmac_f32_e32 v77, v85, v60
	v_fma_f32 v59, -v59, v77, v61
	v_div_fmas_f32 v59, v59, v60, v77
	v_div_fixup_f32 v100, v59, v58, 1.0
	v_pk_mul_f32 v[58:59], v[110:111], v[100:101] op_sel_hi:[1,0]
	v_pk_mul_f32 v[60:61], v[140:141], v[100:101] op_sel_hi:[1,0]
	v_pk_mul_f32 v[58:59], v[28:29], v[58:59]
	v_pk_mul_f32 v[60:61], v[30:31], v[60:61]
	v_pk_mul_f32 v[52:53], v[52:53], v[100:101] op_sel_hi:[1,0]
	global_store_dwordx4 v[42:43], v[58:61], off offset:-4096 nt
	s_nop 1
	v_pk_mul_f32 v[58:59], v[24:25], v[52:53]
	v_pk_mul_f32 v[52:53], v[64:65], v[100:101] op_sel_hi:[1,0]
	s_nop 0
	v_pk_mul_f32 v[60:61], v[26:27], v[52:53]
	v_pk_mul_f32 v[52:53], v[74:75], v[100:101] op_sel_hi:[1,0]
	global_store_dwordx4 v[42:43], v[58:61], off offset:-3072 nt
	s_nop 1
	v_pk_mul_f32 v[58:59], v[20:21], v[52:53]
	v_pk_mul_f32 v[52:53], v[70:71], v[100:101] op_sel_hi:[1,0]
	s_nop 0
	v_pk_mul_f32 v[60:61], v[22:23], v[52:53]
	v_pk_mul_f32 v[52:53], v[88:89], v[100:101] op_sel_hi:[1,0]
	global_store_dwordx4 v[42:43], v[58:61], off offset:-2048 nt
	s_nop 1
	v_pk_mul_f32 v[58:59], v[16:17], v[52:53]
	v_pk_mul_f32 v[52:53], v[80:81], v[100:101] op_sel_hi:[1,0]
	s_nop 0
	v_pk_mul_f32 v[60:61], v[18:19], v[52:53]
	global_store_dwordx4 v[42:43], v[58:61], off offset:-1024 nt
	v_pk_mul_f32 v[52:53], v[134:135], v[100:101] op_sel_hi:[1,0]
	s_nop 0
	v_pk_mul_f32 v[58:59], v[82:83], v[100:101] op_sel_hi:[1,0]
	s_nop 0
	v_pk_mul_f32 v[60:61], v[14:15], v[58:59]
	v_pk_mul_f32 v[58:59], v[12:13], v[52:53]
	global_store_dwordx4 v[42:43], v[58:61], off nt
	v_pk_mul_f32 v[52:53], v[102:103], v[100:101] op_sel_hi:[1,0]
	s_nop 0
	v_pk_mul_f32 v[58:59], v[136:137], v[100:101] op_sel_hi:[1,0]
	s_nop 0
	v_pk_mul_f32 v[60:61], v[10:11], v[58:59]
	v_pk_mul_f32 v[58:59], v[8:9], v[52:53]
	global_store_dwordx4 v[42:43], v[58:61], off offset:1024 nt
	v_pk_mul_f32 v[52:53], v[94:95], v[100:101] op_sel_hi:[1,0]
	s_nop 0
	v_pk_mul_f32 v[58:59], v[98:99], v[100:101] op_sel_hi:[1,0]
	s_nop 0
	v_pk_mul_f32 v[60:61], v[6:7], v[58:59]
	v_pk_mul_f32 v[58:59], v[4:5], v[52:53]
	v_pk_mul_f32 v[52:53], v[104:105], v[100:101] op_sel_hi:[1,0]
	global_store_dwordx4 v[42:43], v[58:61], off offset:2048 nt
	s_nop 1
	v_pk_mul_f32 v[58:59], v[0:1], v[52:53]
	v_pk_mul_f32 v[52:53], v[108:109], v[100:101] op_sel_hi:[1,0]
	s_nop 0
	v_pk_mul_f32 v[60:61], v[2:3], v[52:53]
	global_store_dwordx4 v[42:43], v[58:61], off offset:3072 nt
	s_cbranch_scc1 .LBB0_922
	s_waitcnt vmcnt(34)
	v_cvt_pk_f32_fp8_e32 v[58:59], v84
	v_lshlrev_b32_e32 v64, 16, v50
	v_lshlrev_b32_e32 v192, 16, v66
	v_and_b32_e32 v77, 0xffff0000, v66
	s_waitcnt vmcnt(33)
	v_cvt_pk_f32_fp8_e32 v[60:61], v78
	v_add_f32_e32 v66, v58, v64
	v_cvt_pk_f32_fp8_sdwa v[64:65], v78 src0_sel:WORD_1
	v_and_b32_e32 v50, 0xffff0000, v50
	v_lshlrev_b32_e32 v70, 16, v68
	v_and_b32_e32 v68, 0xffff0000, v68
	v_lshlrev_b32_e32 v71, 16, v69
	v_and_b32_e32 v69, 0xffff0000, v69
	v_lshlrev_b32_e32 v85, 16, v67
	v_and_b32_e32 v83, 0xffff0000, v67
	v_cvt_pk_f32_fp8_e32 v[88:89], v132
	v_cvt_pk_f32_fp8_sdwa v[94:95], v132 src0_sel:WORD_1
	v_cvt_pk_f32_fp8_e32 v[100:101], v57
	v_cvt_pk_f32_fp8_sdwa v[102:103], v57 src0_sel:WORD_1
	v_cvt_pk_f32_fp8_e32 v[104:105], v56
	v_cvt_pk_f32_fp8_sdwa v[108:109], v56 src0_sel:WORD_1
	v_cvt_pk_f32_fp8_e32 v[56:57], v79
	v_cvt_pk_f32_fp8_sdwa v[110:111], v79 src0_sel:WORD_1
	v_add_f32_e32 v50, v59, v50
	v_add_f32_e32 v67, v61, v68
	v_add_f32_e32 v82, v64, v71
	v_add_f32_e32 v68, v65, v69
	s_waitcnt vmcnt(32)
	v_cvt_pk_f32_fp8_e32 v[78:79], v125
	v_cvt_pk_f32_fp8_sdwa v[132:133], v125 src0_sel:WORD_1
	s_waitcnt vmcnt(26)
	v_cvt_pk_f32_fp8_e32 v[64:65], v124
	v_cvt_pk_f32_fp8_sdwa v[58:59], v124 src0_sel:WORD_1
	s_waitcnt vmcnt(25)
	v_cvt_pk_f32_fp8_e32 v[124:125], v76
	v_cvt_pk_f32_fp8_sdwa v[146:147], v76 src0_sel:WORD_1
	s_waitcnt vmcnt(17)
	v_cvt_pk_f32_fp8_e32 v[166:167], v63
	v_cvt_pk_f32_fp8_sdwa v[168:169], v63 src0_sel:WORD_1
	v_cvt_pk_f32_fp8_e32 v[80:81], v131
	v_cvt_pk_f32_fp8_sdwa v[98:99], v131 src0_sel:WORD_1
	v_add_f32_e32 v76, v66, v64
	v_add_f32_e32 v66, v67, v125
	v_add_f32_e32 v67, v68, v147
	s_waitcnt vmcnt(16)
	v_cvt_pk_f32_fp8_e32 v[68:69], v87
	v_cvt_pk_f32_fp8_sdwa v[170:171], v87 src0_sel:WORD_1
	s_waitcnt vmcnt(9)
	v_cvt_pk_f32_fp8_e32 v[186:187], v86
	v_cvt_pk_f32_fp8_sdwa v[86:87], v86 src0_sel:WORD_1
	v_cvt_pk_f32_fp8_e32 v[136:137], v129
	v_cvt_pk_f32_fp8_sdwa v[138:139], v129 src0_sel:WORD_1
	v_cvt_pk_f32_fp8_e32 v[152:153], v123
	v_cvt_pk_f32_fp8_sdwa v[154:155], v123 src0_sel:WORD_1
	v_cvt_pk_f32_fp8_e32 v[156:157], v122
	v_cvt_pk_f32_fp8_sdwa v[122:123], v122 src0_sel:WORD_1
	v_add_f32_e32 v66, v66, v167
	v_add_f32_e32 v67, v67, v169
	v_cvt_pk_f32_fp8_e32 v[174:175], v93
	v_cvt_pk_f32_fp8_sdwa v[176:177], v93 src0_sel:WORD_1
	v_cvt_pk_f32_fp8_sdwa v[52:53], v84 src0_sel:WORD_1
	v_add_f32_e32 v84, v60, v70
	v_cvt_pk_f32_fp8_e32 v[184:185], v73
	v_cvt_pk_f32_fp8_sdwa v[70:71], v73 src0_sel:WORD_1
	v_add_f32_e32 v194, v66, v187
	v_add_f32_e32 v195, v67, v87
	s_waitcnt vmcnt(8)
	v_cvt_pk_f32_fp8_e32 v[66:67], v72
	v_cvt_pk_f32_fp8_sdwa v[188:189], v72 src0_sel:WORD_1
	v_lshlrev_b32_e32 v73, 16, v49
	v_lshlrev_b32_e32 v72, 16, v48
	v_and_b32_e32 v49, 0xffff0000, v49
	v_and_b32_e32 v48, 0xffff0000, v48
	v_mov_b32_e32 v190, v80
	v_mov_b32_e32 v191, v98
	v_mov_b32_e32 v98, v81
	v_pk_add_f32 v[72:73], v[190:191], v[72:73]
	v_pk_add_f32 v[48:49], v[98:99], v[48:49]
	v_mov_b32_e32 v80, v136
	v_mov_b32_e32 v81, v138
	v_mov_b32_e32 v138, v137
	v_pk_add_f32 v[72:73], v[72:73], v[80:81]
	v_pk_add_f32 v[48:49], v[48:49], v[138:139]
	v_mov_b32_e32 v80, v156
	v_mov_b32_e32 v81, v122
	v_mov_b32_e32 v122, v157
	v_pk_add_f32 v[72:73], v[72:73], v[80:81]
	v_pk_add_f32 v[48:49], v[48:49], v[122:123]
	v_mov_b32_e32 v81, v176
	v_mov_b32_e32 v176, v175
	v_cvt_pk_f32_fp8_e32 v[140:141], v128
	v_cvt_pk_f32_fp8_sdwa v[128:129], v128 src0_sel:WORD_1
	v_mov_b32_e32 v80, v174
	v_pk_add_f32 v[48:49], v[48:49], v[176:177]
	v_cvt_pk_f32_fp8_e32 v[158:159], v121
	v_cvt_pk_f32_fp8_sdwa v[160:161], v121 src0_sel:WORD_1
	v_pk_add_f32 v[72:73], v[72:73], v[80:81]
	v_pk_mul_f32 v[80:81], v[48:49], v[48:49]
	v_cvt_pk_f32_fp8_e32 v[178:179], v92
	v_cvt_pk_f32_fp8_sdwa v[92:93], v92 src0_sel:WORD_1
	v_pk_fma_f32 v[80:81], v[72:73], v[72:73], v[80:81]
	v_mov_b32_e32 v122, v100
	v_pk_add_f32 v[98:99], v[80:81], v[80:81] op_sel:[0,1] op_sel_hi:[1,0]
	v_lshlrev_b32_e32 v81, 16, v47
	v_lshlrev_b32_e32 v80, 16, v46
	v_and_b32_e32 v47, 0xffff0000, v47
	v_and_b32_e32 v46, 0xffff0000, v46
	v_mov_b32_e32 v123, v102
	v_mov_b32_e32 v102, v101
	v_pk_add_f32 v[80:81], v[122:123], v[80:81]
	v_pk_add_f32 v[46:47], v[102:103], v[46:47]
	v_mov_b32_e32 v100, v140
	v_mov_b32_e32 v101, v128
	v_mov_b32_e32 v128, v141
	v_pk_add_f32 v[80:81], v[80:81], v[100:101]
	v_pk_add_f32 v[46:47], v[46:47], v[128:129]
	v_mov_b32_e32 v100, v158
	v_mov_b32_e32 v101, v160
	v_mov_b32_e32 v160, v159
	v_pk_add_f32 v[80:81], v[80:81], v[100:101]
	v_pk_add_f32 v[46:47], v[46:47], v[160:161]
	v_mov_b32_e32 v101, v92
	v_mov_b32_e32 v92, v179
	v_cvt_pk_f32_fp8_e32 v[142:143], v127
	v_cvt_pk_f32_fp8_sdwa v[144:145], v127 src0_sel:WORD_1
	v_mov_b32_e32 v100, v178
	v_pk_add_f32 v[46:47], v[46:47], v[92:93]
	v_cvt_pk_f32_fp8_e32 v[162:163], v120
	v_cvt_pk_f32_fp8_sdwa v[120:121], v120 src0_sel:WORD_1
	v_pk_add_f32 v[100:101], v[80:81], v[100:101]
	v_pk_mul_f32 v[80:81], v[46:47], v[46:47]
	v_cvt_pk_f32_fp8_e32 v[180:181], v91
	v_cvt_pk_f32_fp8_sdwa v[182:183], v91 src0_sel:WORD_1
	v_pk_fma_f32 v[80:81], v[100:101], v[100:101], v[80:81]
	v_mov_b32_e32 v102, v104
	v_pk_add_f32 v[92:93], v[80:81], v[80:81] op_sel:[0,1] op_sel_hi:[1,0]
	v_lshlrev_b32_e32 v81, 16, v35
	v_lshlrev_b32_e32 v80, 16, v34
	v_and_b32_e32 v35, 0xffff0000, v35
	v_and_b32_e32 v34, 0xffff0000, v34
	v_mov_b32_e32 v103, v108
	v_mov_b32_e32 v108, v105
	v_pk_add_f32 v[80:81], v[102:103], v[80:81]
	v_pk_add_f32 v[34:35], v[108:109], v[34:35]
	v_mov_b32_e32 v102, v142
	v_mov_b32_e32 v103, v144
	v_mov_b32_e32 v144, v143
	v_pk_add_f32 v[80:81], v[80:81], v[102:103]
	v_pk_add_f32 v[34:35], v[34:35], v[144:145]
	v_mov_b32_e32 v102, v162
	v_mov_b32_e32 v103, v120
	v_mov_b32_e32 v120, v163
	v_pk_add_f32 v[80:81], v[80:81], v[102:103]
	v_pk_add_f32 v[34:35], v[34:35], v[120:121]
	v_mov_b32_e32 v103, v182
	v_mov_b32_e32 v182, v181
	v_mov_b32_e32 v102, v180
	v_pk_add_f32 v[34:35], v[34:35], v[182:183]
	v_pk_add_f32 v[102:103], v[80:81], v[102:103]
	v_pk_mul_f32 v[80:81], v[34:35], v[34:35]
	v_cvt_pk_f32_fp8_e32 v[134:135], v130
	v_pk_fma_f32 v[80:81], v[102:103], v[102:103], v[80:81]
	v_cvt_pk_f32_fp8_e32 v[172:173], v96
	v_pk_add_f32 v[104:105], v[80:81], v[80:81] op_sel:[0,1] op_sel_hi:[1,0]
	v_lshlrev_b32_e32 v80, 16, v55
	v_and_b32_e32 v81, 0xffff0000, v55
	v_pk_add_f32 v[80:81], v[110:111], v[80:81]
	v_lshlrev_b32_e32 v110, 16, v32
	v_and_b32_e32 v111, 0xffff0000, v32
	v_pk_add_f32 v[88:89], v[88:89], v[110:111]
	v_cvt_pk_f32_fp8_sdwa v[130:131], v130 src0_sel:WORD_1
	v_pk_add_f32 v[88:89], v[88:89], v[134:135]
	v_cvt_pk_f32_fp8_e32 v[148:149], v97
	v_pk_add_f32 v[88:89], v[88:89], v[152:153]
	v_cvt_pk_f32_fp8_sdwa v[150:151], v97 src0_sel:WORD_1
	v_pk_add_f32 v[88:89], v[88:89], v[172:173]
	v_cvt_pk_f32_fp8_sdwa v[96:97], v96 src0_sel:WORD_1
	v_mul_f32_e32 v32, v89, v89
	v_pk_fma_f32 v[110:111], v[88:89], v[88:89], v[32:33] op_sel_hi:[1,1,0]
	v_lshlrev_b32_e32 v32, 16, v33
	v_and_b32_e32 v33, 0xffff0000, v33
	v_pk_add_f32 v[32:33], v[94:95], v[32:33]
	v_cvt_pk_f32_fp8_e32 v[164:165], v62
	v_pk_add_f32 v[32:33], v[32:33], v[130:131]
	v_add_f32_e32 v50, v50, v65
	v_pk_add_f32 v[32:33], v[32:33], v[154:155]
	v_mov_b32_e32 v111, v78
	v_pk_add_f32 v[32:33], v[32:33], v[96:97]
	v_add_f32_e32 v50, v50, v165
	v_mul_f32_e32 v78, v33, v33
	v_mov_b32_e32 v165, v79
	v_pk_fma_f32 v[78:79], v[32:33], v[32:33], v[78:79] op_sel_hi:[1,1,0]
	v_mov_b32_e32 v147, v133
	v_mov_b32_e32 v79, v192
	v_cvt_pk_f32_fp8_e32 v[60:61], v126
	v_cvt_pk_f32_fp8_sdwa v[126:127], v126 src0_sel:WORD_1
	v_pk_add_f32 v[82:83], v[82:83], v[146:147]
	v_mov_b32_e32 v169, v151
	v_pk_add_f32 v[78:79], v[110:111], v[78:79]
	v_mov_b32_e32 v99, v148
	v_cvt_pk_f32_fp8_e32 v[64:65], v106
	v_cvt_pk_f32_fp8_sdwa v[106:107], v106 src0_sel:WORD_1
	v_pk_add_f32 v[82:83], v[82:83], v[168:169]
	v_mov_b32_e32 v87, v171
	v_pk_add_f32 v[78:79], v[78:79], v[98:99]
	v_mov_b32_e32 v93, v68
	v_cvt_pk_f32_fp8_e32 v[74:75], v90
	v_cvt_pk_f32_fp8_sdwa v[90:91], v90 src0_sel:WORD_1
	v_pk_add_f32 v[82:83], v[82:83], v[86:87]
	v_pk_add_f32 v[86:87], v[78:79], v[92:93]
	v_mov_b32_e32 v105, v66
	v_pk_add_f32 v[86:87], v[86:87], v[104:105]
	v_lshlrev_b32_e32 v104, 16, v54
	v_and_b32_e32 v105, 0xffff0000, v54
	v_add_f32_e32 v193, v50, v185
	v_pk_add_f32 v[80:81], v[80:81], v[126:127]
	v_pk_add_f32 v[76:77], v[76:77], v[164:165]
	v_mov_b32_e32 v185, v149
	v_pk_add_f32 v[54:55], v[56:57], v[104:105]
	v_pk_add_f32 v[80:81], v[80:81], v[106:107]
	v_mov_b32_e32 v125, v132
	v_pk_add_f32 v[76:77], v[76:77], v[184:185]
	v_pk_add_f32 v[54:55], v[54:55], v[60:61]
	v_pk_add_f32 v[80:81], v[80:81], v[90:91]
	v_pk_add_f32 v[84:85], v[84:85], v[124:125]
	v_mov_b32_e32 v167, v150
	v_mov_b32_e32 v92, v76
	v_mov_b32_e32 v93, v69
	v_pk_add_f32 v[54:55], v[54:55], v[64:65]
	v_mul_f32_e32 v50, v81, v81
	v_pk_add_f32 v[84:85], v[84:85], v[166:167]
	v_mov_b32_e32 v187, v170
	v_pk_mul_f32 v[94:95], v[76:77], v[76:77]
	v_pk_add_f32 v[92:93], v[76:77], v[92:93]
	v_pk_add_f32 v[54:55], v[54:55], v[74:75]
	v_cvt_pk_f32_fp8_sdwa v[62:63], v62 src0_sel:WORD_1
	v_pk_fma_f32 v[90:91], v[80:81], v[80:81], v[50:51] op_sel_hi:[1,1,0]
	v_mul_f32_e32 v106, v193, v193
	v_mul_f32_e32 v50, v194, v194
	v_pk_add_f32 v[84:85], v[84:85], v[186:187]
	v_mov_b32_e32 v95, v93
	v_mov_b32_e32 v107, v67
	v_pk_mul_f32 v[56:57], v[54:55], v[54:55]
	v_pk_add_f32 v[94:95], v[94:95], v[106:107]
	v_pk_fma_f32 v[106:107], v[84:85], v[84:85], v[50:51]
	v_mov_b32_e32 v78, v56
	v_pk_mov_b32 v[56:57], v[56:57], v[68:69] op_sel:[1,0]
	v_lshlrev_b32_e32 v50, 16, v51
	v_and_b32_e32 v51, 0xffff0000, v51
	v_mov_b32_e32 v91, v66
	v_pk_add_f32 v[56:57], v[78:79], v[56:57]
	v_pk_add_f32 v[50:51], v[52:53], v[50:51]
	v_pk_add_f32 v[56:57], v[56:57], v[90:91]
	v_pk_add_f32 v[50:51], v[50:51], v[58:59]
	v_pk_add_f32 v[60:61], v[86:87], v[56:57]
	v_pk_mul_f32 v[56:57], v[86:87], v[56:57]
	v_pk_add_f32 v[50:51], v[50:51], v[62:63]
	v_mov_b32_e32 v61, v57
	v_pk_add_f32 v[56:57], v[50:51], v[70:71]
	v_mov_b32_e32 v96, v84
	v_mov_b32_e32 v97, v188
	v_pk_mul_f32 v[50:51], v[56:57], v[56:57]
	v_pk_add_f32 v[96:97], v[84:85], v[96:97]
	v_mov_b32_e32 v188, v82
	v_mov_b32_e32 v92, v50
	v_mov_b32_e32 v66, v51
	v_mul_f32_e32 v108, v195, v195
	v_pk_add_f32 v[98:99], v[82:83], v[188:189]
	v_pk_mul_f32 v[110:111], v[96:97], v[96:97]
	v_pk_add_f32 v[50:51], v[92:93], v[66:67]
	v_mov_b32_e32 v107, v111
	v_pk_fma_f32 v[108:109], v[82:83], v[82:83], v[108:109]
	v_pk_mul_f32 v[110:111], v[98:99], v[98:99]
	v_pk_add_f32 v[52:53], v[94:95], v[50:51]
	v_pk_mul_f32 v[50:51], v[94:95], v[50:51]
	v_mov_b32_e32 v109, v111
	v_mov_b32_e32 v53, v51
	v_pk_add_f32 v[106:107], v[106:107], v[108:109]
	v_pk_add_f32 v[50:51], v[60:61], v[52:53]
	s_lshl_b64 s[0:1], s[12:13], 13
	v_pk_add_f32 v[50:51], v[50:51], v[106:107]
	v_lshl_add_u64 v[58:59], v[40:41], 0, s[0:1]
	v_add_f32_e32 v50, v50, v51
	ds_bpermute_b32 v51, v112, v50
	v_mov_b32_e32 v60, v72
	v_mov_b32_e32 v61, v48
	v_mov_b32_e32 v48, v73
	v_mov_b32_e32 v62, v100
	s_waitcnt lgkmcnt(0)
	v_add_f32_e32 v50, v50, v51
	ds_bpermute_b32 v51, v113, v50
	v_mov_b32_e32 v63, v46
	v_mov_b32_e32 v46, v101
	v_mov_b32_e32 v64, v102
	v_mov_b32_e32 v65, v34
	s_waitcnt lgkmcnt(0)
	v_add_f32_e32 v50, v50, v51
	ds_bpermute_b32 v51, v114, v50
	v_mov_b32_e32 v34, v103
	v_mov_b32_e32 v77, v193
	v_mov_b32_e32 v85, v194
	v_mov_b32_e32 v83, v195
	s_waitcnt lgkmcnt(0)
	v_add_f32_e32 v50, v50, v51
	ds_bpermute_b32 v51, v115, v50
	v_mov_b32_e32 v94, v87
	v_mov_b32_e32 v98, v97
	s_waitcnt lgkmcnt(0)
	v_add_f32_e32 v50, v50, v51
	ds_bpermute_b32 v51, v116, v50
	s_waitcnt lgkmcnt(0)
	v_add_f32_e32 v50, v50, v51
	ds_bpermute_b32 v51, v117, v50
	s_waitcnt lgkmcnt(0)
	v_add_f32_e32 v50, v50, v51
	v_fmamk_f32 v50, v50, 0x3a000000, v118
	v_mul_f32_e32 v51, 0x4f800000, v50
	v_cmp_gt_f32_e32 vcc, s20, v50
	s_nop 1
	v_cndmask_b32_e32 v50, v50, v51, vcc
	v_sqrt_f32_e32 v51, v50
	s_nop 0
	v_add_u32_e32 v52, -1, v51
	v_fma_f32 v53, -v52, v51, v50
	v_cmp_ge_f32_e64 s[0:1], 0, v53
	v_add_u32_e32 v53, 1, v51
	s_nop 0
	v_cndmask_b32_e64 v52, v51, v52, s[0:1]
	v_fma_f32 v51, -v53, v51, v50
	v_cmp_lt_f32_e64 s[0:1], 0, v51
	s_nop 1
	v_cndmask_b32_e64 v51, v52, v53, s[0:1]
	v_mul_f32_e32 v52, 0x37800000, v51
	v_cndmask_b32_e32 v51, v51, v52, vcc
	v_cmp_class_f32_e32 vcc, v50, v119
	s_nop 1
	v_cndmask_b32_e32 v50, v51, v50, vcc
	v_div_scale_f32 v51, s[0:1], v50, v50, 1.0
	v_rcp_f32_e32 v52, v51
	s_nop 0
	v_fma_f32 v53, -v51, v52, 1.0
	v_fmac_f32_e32 v52, v53, v52
	v_div_scale_f32 v53, vcc, 1.0, v50, 1.0
	v_mul_f32_e32 v66, v53, v52
	v_fma_f32 v67, -v51, v66, v53
	v_fmac_f32_e32 v66, v67, v52
	v_fma_f32 v51, -v51, v66, v53
	v_div_fmas_f32 v51, v51, v52, v66
	v_div_fixup_f32 v66, v51, v50, 1.0
	v_pk_mul_f32 v[50:51], v[88:89], v[66:67] op_sel_hi:[1,0]
	v_pk_mul_f32 v[32:33], v[32:33], v[66:67] op_sel_hi:[1,0]
	v_pk_mul_f32 v[50:51], v[28:29], v[50:51]
	v_pk_mul_f32 v[52:53], v[30:31], v[32:33]
	v_pk_mul_f32 v[32:33], v[60:61], v[66:67] op_sel_hi:[1,0]
	global_store_dwordx4 v[58:59], v[50:53], off nt
	v_pk_mul_f32 v[34:35], v[34:35], v[66:67] op_sel_hi:[1,0]
	s_nop 0
	v_pk_mul_f32 v[50:51], v[24:25], v[32:33]
	v_pk_mul_f32 v[32:33], v[48:49], v[66:67] op_sel_hi:[1,0]
	v_pk_mul_f32 v[34:35], v[18:19], v[34:35]
	v_pk_mul_f32 v[52:53], v[26:27], v[32:33]
	v_pk_mul_f32 v[32:33], v[62:63], v[66:67] op_sel_hi:[1,0]
	global_store_dwordx4 v[58:59], v[50:53], off offset:1024 nt
	v_pk_mul_f32 v[48:49], v[20:21], v[32:33]
	v_pk_mul_f32 v[32:33], v[46:47], v[66:67] op_sel_hi:[1,0]
	v_add_co_u32_e32 v46, vcc, s18, v58
	v_pk_mul_f32 v[50:51], v[22:23], v[32:33]
	v_pk_mul_f32 v[32:33], v[64:65], v[66:67] op_sel_hi:[1,0]
	v_addc_co_u32_e32 v47, vcc, 0, v59, vcc
	v_pk_mul_f32 v[32:33], v[16:17], v[32:33]
	global_store_dwordx4 v[58:59], v[32:35], off offset:3072 nt
	global_store_dwordx4 v[58:59], v[48:51], off offset:2048 nt
	s_nop 0
	v_pk_mul_f32 v[32:33], v[54:55], v[66:67] op_sel_hi:[1,0]
	v_pk_mul_f32 v[34:35], v[80:81], v[66:67] op_sel_hi:[1,0]
	v_pk_mul_f32 v[32:33], v[12:13], v[32:33]
	v_pk_mul_f32 v[34:35], v[14:15], v[34:35]
	global_store_dwordx4 v[46:47], v[32:35], off nt
	s_nop 1
	v_pk_mul_f32 v[32:33], v[76:77], v[66:67] op_sel_hi:[1,0]
	v_pk_mul_f32 v[34:35], v[56:57], v[66:67] op_sel_hi:[1,0]
	v_pk_mul_f32 v[32:33], v[8:9], v[32:33]
	v_pk_mul_f32 v[34:35], v[10:11], v[34:35]
	global_store_dwordx4 v[46:47], v[32:35], off offset:1024 nt
	s_nop 1
	v_pk_mul_f32 v[32:33], v[84:85], v[66:67] op_sel_hi:[1,0]
	v_pk_mul_f32 v[34:35], v[82:83], v[66:67] op_sel_hi:[1,0]
	v_pk_mul_f32 v[32:33], v[4:5], v[32:33]
	v_pk_mul_f32 v[34:35], v[6:7], v[34:35]
	global_store_dwordx4 v[46:47], v[32:35], off offset:2048 nt
	s_nop 1
	v_pk_mul_f32 v[32:33], v[94:95], v[66:67] op_sel_hi:[1,0]
	v_pk_mul_f32 v[34:35], v[98:99], v[66:67] op_sel_hi:[1,0]
	v_pk_mul_f32 v[32:33], v[0:1], v[32:33]
	v_pk_mul_f32 v[34:35], v[2:3], v[34:35]
	global_store_dwordx4 v[46:47], v[32:35], off offset:3072 nt
	s_branch .LBB0_922
